# speedup vs baseline: 1.0109x; 1.0109x over previous
_Z6k_attnPKDF16_PKfPDF16_:
	s_load_dwordx4 s[4:7], s[0:1], 0x0
	s_load_dwordx2 s[8:9], s[0:1], 0x10
	s_lshr_b32 s0, s2, 3
	s_sub_i32 s0, 0x2ff, s0
	s_lshl_b32 s1, s2, 5
	s_mul_hi_i32 s2, s0, 0x2aaaaaab
	s_lshr_b32 s3, s2, 31
	s_ashr_i32 s2, s2, 2
	s_and_b32 s1, s1, 0xe0
	s_add_i32 s2, s2, s3
	s_add_i32 s1, s2, s1
	s_mul_i32 s2, s2, 24
	s_sub_i32 s0, s0, s2
	s_mul_i32 s2, s0, 43
	s_bfe_u32 s3, s2, 0x1000f
	s_bfe_u32 s2, s2, 0x80008
	s_add_i32 s2, s2, s3
	s_sext_i32_i8 s2, s2
	s_mul_i32 s3, s2, -6
	s_add_i32 s3, s3, s0
	s_lshl_b32 s0, s1, 2
	s_add_i32 s2, s0, s2
	s_mul_i32 s1, s2, 0x48000
	s_mul_hi_i32 s0, s2, 0x48000
	s_waitcnt lgkmcnt(0)
	s_add_u32 s4, s4, s1
	s_addc_u32 s5, s5, s0
	s_lshl_b32 s0, s3, 7
	s_ashr_i32 s1, s0, 31
	s_lshl_b64 s[0:1], s[0:1], 1
	s_add_u32 s4, s4, s0
	v_lshlrev_b32_e32 v2, 4, v0
	v_lshrrev_b32_e32 v9, 4, v0
	s_addc_u32 s5, s5, s1
	v_and_b32_e32 v2, 0xf0, v2
	v_mov_b32_e32 v3, 0
	v_mul_u32_u24_e32 v6, 0x900, v9
	v_lshl_add_u64 v[4:5], s[4:5], 0, v[2:3]
	v_lshlrev_b32_e32 v6, 1, v6
	v_mov_b32_e32 v7, v3
	v_lshl_add_u64 v[6:7], v[4:5], 0, v[6:7]
	global_load_dwordx4 v[10:13], v[6:7], off offset:1536 nt
	global_load_dwordx4 v[14:17], v[6:7], off offset:3072 nt
	v_or_b32_e32 v6, 0x100, v0
	v_lshrrev_b32_e32 v50, 4, v6
	v_mul_u32_u24_e32 v6, 0x900, v50
	v_lshlrev_b32_e32 v6, 1, v6
	v_mov_b32_e32 v7, v3
	v_lshl_add_u64 v[6:7], v[4:5], 0, v[6:7]
	global_load_dwordx4 v[18:21], v[6:7], off offset:1536 nt
	global_load_dwordx4 v[22:25], v[6:7], off offset:3072 nt
	v_or_b32_e32 v6, 0x200, v0
	v_lshrrev_b32_e32 v51, 4, v6
	v_mul_u32_u24_e32 v6, 0x900, v51
	v_lshlrev_b32_e32 v6, 1, v6
	v_mov_b32_e32 v7, v3
	v_lshl_add_u64 v[6:7], v[4:5], 0, v[6:7]
	global_load_dwordx4 v[26:29], v[6:7], off offset:1536 nt
	global_load_dwordx4 v[30:33], v[6:7], off offset:3072 nt
	v_or_b32_e32 v6, 0x300, v0
	v_lshrrev_b32_e32 v52, 4, v6
	v_mul_u32_u24_e32 v6, 0x900, v52
	v_lshlrev_b32_e32 v6, 1, v6
	v_mov_b32_e32 v7, v3
	v_lshrrev_b32_e32 v1, 6, v0
	v_lshl_add_u64 v[4:5], v[4:5], 0, v[6:7]
	v_and_b32_e32 v8, 15, v0
	global_load_dwordx4 v[34:37], v[4:5], off offset:1536 nt
	global_load_dwordx4 v[38:41], v[4:5], off offset:3072 nt
	v_lshlrev_b32_e32 v6, 4, v1
	v_or_b32_e32 v4, v6, v8
	v_mul_u32_u24_e32 v4, 0x900, v4
	v_lshlrev_b32_e32 v4, 1, v4
	v_mov_b32_e32 v5, v3
	v_lshl_add_u64 v[4:5], s[4:5], 0, v[4:5]
	v_and_b32_e32 v58, 48, v0
	v_mov_b32_e32 v59, v3
	v_lshl_add_u64 v[4:5], v[4:5], 0, v[58:59]
	global_load_dwordx4 v[42:45], v[4:5], off nt
	global_load_dwordx4 v[46:49], v[4:5], off offset:64 nt
	s_movk_i32 s3, 0x110
	s_movk_i32 s4, 0x120
	v_or_b32_e32 v7, 0x4800, v2
	v_mad_u32_u24 v59, v9, s4, v2
	v_mad_u32_u24 v9, v9, s3, v7
	v_mad_u32_u24 v60, v50, s4, v2
	v_mad_u32_u24 v61, v51, s4, v2
	v_mad_u32_u24 v62, v52, s4, v2
	v_mad_u32_u24 v63, v50, s3, v7
	v_mad_u32_u24 v64, v51, s3, v7
	v_mad_u32_u24 v7, v52, s3, v7
	global_load_dwordx4 v[50:53], v[4:5], off offset:128 nt
	global_load_dwordx4 v[54:57], v[4:5], off offset:192 nt
	v_lshlrev_b32_e32 v4, 2, v8
	v_mov_b32_e32 v5, v3
	v_lshl_add_u64 v[4:5], s[6:7], 0, v[4:5]
	s_movk_i32 s4, 0x900
	s_waitcnt vmcnt(11)
	ds_write_b128 v9, v[10:13]
	s_waitcnt vmcnt(10)
	ds_write_b128 v59, v[14:17]
	s_waitcnt vmcnt(9)
	ds_write_b128 v63, v[18:21]
	s_waitcnt vmcnt(8)
	ds_write_b128 v60, v[22:25]
	s_waitcnt vmcnt(7)
	ds_write_b128 v64, v[26:29]
	s_waitcnt vmcnt(6)
	ds_write_b128 v61, v[30:33]
	s_waitcnt vmcnt(5)
	ds_write_b128 v7, v[34:37]
	s_waitcnt vmcnt(4)
	ds_write_b128 v62, v[38:41]
	v_mad_u32_u24 v30, v8, s3, v58
	s_waitcnt lgkmcnt(0)
	s_barrier
	ds_read_b128 v[10:13], v30 offset:18432
	ds_read_b128 v[14:17], v30 offset:18496
	s_waitcnt vmcnt(3) lgkmcnt(1)
	v_mfma_f32_16x16x32_f16 a[0:3], v[42:45], v[10:13], 0
	v_bfe_u32 v7, v0, 4, 2
	v_lshlrev_b32_e32 v9, 2, v7
	v_mbcnt_lo_u32_b32 v39, -1, 0
	s_waitcnt vmcnt(2) lgkmcnt(0)
	v_mfma_f32_16x16x32_f16 a[0:3], v[46:49], v[14:17], a[0:3]
	ds_read_b128 v[10:13], v30 offset:22784
	ds_read_b128 v[14:17], v30 offset:22848
	s_waitcnt lgkmcnt(1)
	v_mfma_f32_16x16x32_f16 a[4:7], v[42:45], v[10:13], 0
	s_waitcnt lgkmcnt(0)
	v_mfma_f32_16x16x32_f16 a[4:7], v[46:49], v[14:17], a[4:7]
	ds_read_b128 v[10:13], v30 offset:27136
	ds_read_b128 v[14:17], v30 offset:27200
	s_waitcnt lgkmcnt(1)
	v_mfma_f32_16x16x32_f16 a[8:11], v[42:45], v[10:13], 0
	ds_read_b128 v[10:13], v30 offset:31488
	s_waitcnt lgkmcnt(1)
	v_mfma_f32_16x16x32_f16 a[8:11], v[46:49], v[14:17], a[8:11]
	ds_read_b128 v[14:17], v30 offset:31552
	s_waitcnt lgkmcnt(1)
	v_mfma_f32_16x16x32_f16 a[12:15], v[42:45], v[10:13], 0
	v_or_b32_e32 v10, v9, v6
	v_lshlrev_b32_e32 v10, 8, v10
	v_mov_b32_e32 v11, v3
	v_lshl_add_u64 v[4:5], v[4:5], 0, v[10:11]
	global_load_dword v31, v[4:5], off
	global_load_dword v32, v[4:5], off offset:64
	global_load_dword v33, v[4:5], off offset:128
	global_load_dword v34, v[4:5], off offset:192
	s_waitcnt lgkmcnt(0)
	v_mfma_f32_16x16x32_f16 a[12:15], v[46:49], v[14:17], a[12:15]
	ds_read_b128 v[10:13], v30 offset:18560
	ds_read_b128 v[14:17], v30 offset:18624
	ds_read_b128 v[18:21], v30 offset:22912
	s_waitcnt vmcnt(5) lgkmcnt(2)
	v_mfma_f32_16x16x32_f16 a[0:3], v[50:53], v[10:13], a[0:3]
	ds_read_b128 v[10:13], v30 offset:22976
	ds_read_b128 v[22:25], v30 offset:27264
	ds_read_b128 v[26:29], v30 offset:27328
	global_load_dword v35, v[4:5], off offset:256
	global_load_dword v36, v[4:5], off offset:320
	global_load_dword v37, v[4:5], off offset:384
	global_load_dword v38, v[4:5], off offset:448
	s_waitcnt lgkmcnt(3)
	v_mfma_f32_16x16x32_f16 a[4:7], v[50:53], v[18:21], a[4:7]
	ds_read_b128 v[18:21], v30 offset:31616
	s_waitcnt lgkmcnt(2)
	v_mfma_f32_16x16x32_f16 a[8:11], v[50:53], v[22:25], a[8:11]
	ds_read_b128 v[22:25], v30 offset:31680
	s_waitcnt lgkmcnt(1)
	v_mfma_f32_16x16x32_f16 a[12:15], v[50:53], v[18:21], a[12:15]
	v_mbcnt_hi_u32_b32 v19, -1, v39
	v_lshlrev_b32_e32 v20, 3, v7
	v_lshlrev_b32_e32 v18, 3, v0
	s_waitcnt vmcnt(8)
	v_mfma_f32_16x16x32_f16 a[8:11], v[54:57], v[26:29], a[8:11]
	v_bfe_u32 v0, v0, 2, 2
	v_or_b32_e32 v0, v9, v0
	v_mul_u32_u24_e32 v0, 0x120, v0
	s_waitcnt lgkmcnt(0)
	v_mfma_f32_16x16x32_f16 a[12:15], v[54:57], v[22:25], a[12:15]
	v_and_or_b32 v0, v18, 24, v0
	v_mfma_f32_16x16x32_f16 a[0:3], v[54:57], v[14:17], a[0:3]
	v_and_b32_e32 v15, 64, v19
	v_xor_b32_e32 v14, 1, v19
	v_accvgpr_read_b32 v17, a8
	v_mfma_f32_16x16x32_f16 a[4:7], v[54:57], v[10:13], a[4:7]
	v_add_u32_e32 v12, 64, v15
	v_cmp_lt_i32_e32 vcc, v14, v12
	v_accvgpr_read_b32 v21, a12
	v_xor_b32_e32 v16, 2, v19
	v_cndmask_b32_e32 v13, v19, v14, vcc
	v_accvgpr_read_b32 v14, a0
	v_lshlrev_b32_e32 v13, 2, v13
	v_cmp_lt_i32_e32 vcc, v16, v12
	v_accvgpr_read_b32 v15, a4
	v_xor_b32_e32 v10, 4, v19
	v_cndmask_b32_e32 v16, v19, v16, vcc
	v_lshlrev_b32_e32 v16, 2, v16
	v_xor_b32_e32 v11, 8, v19
	v_cmp_lt_i32_e32 vcc, v10, v12
	v_accvgpr_read_b32 v26, a9
	v_accvgpr_read_b32 v22, a1
	v_cndmask_b32_e32 v10, v19, v10, vcc
	v_cmp_lt_i32_e32 vcc, v11, v12
	v_lshlrev_b32_e32 v10, 2, v10
	v_accvgpr_read_b32 v25, a5
	v_cndmask_b32_e32 v11, v19, v11, vcc
	v_lshlrev_b32_e32 v11, 2, v11
	v_accvgpr_read_b32 v41, a14
	v_accvgpr_read_b32 v23, a2
	v_accvgpr_read_b32 v42, a15
	v_accvgpr_read_b32 v24, a3
	s_waitcnt vmcnt(7)
	v_fmac_f32_e32 v31, 0x3e0293ee, v14
	s_waitcnt vmcnt(6)
	v_fmac_f32_e32 v32, 0x3e0293ee, v15
	s_waitcnt vmcnt(5)
	v_fmac_f32_e32 v33, 0x3e0293ee, v17
	s_waitcnt vmcnt(4)
	v_fmac_f32_e32 v34, 0x3e0293ee, v21
	v_max_f32_e32 v14, v33, v34
	v_max3_f32 v14, v31, v32, v14
	s_nop 1
	v_mov_b32_dpp v15, v14 quad_perm:[1,0,3,2] row_mask:0xf bank_mask:0xf
	s_waitcnt vmcnt(3)
	v_fmac_f32_e32 v35, 0x3e0293ee, v22
	s_waitcnt vmcnt(2)
	v_fmac_f32_e32 v36, 0x3e0293ee, v25
	s_waitcnt vmcnt(1)
	v_fmac_f32_e32 v37, 0x3e0293ee, v26
	s_waitcnt lgkmcnt(0)
	v_max_f32_e32 v15, v15, v15
	v_max_f32_e32 v14, v14, v15
	s_nop 1
	v_mov_b32_dpp v15, v14 quad_perm:[2,3,0,1] row_mask:0xf bank_mask:0xf
	s_waitcnt lgkmcnt(0)
	v_max_f32_e32 v12, v15, v15
	global_load_dword v15, v[4:5], off offset:512
	global_load_dword v17, v[4:5], off offset:576
	global_load_dword v19, v[4:5], off offset:640
	global_load_dword v21, v[4:5], off offset:704
	v_max_f32_e32 v12, v14, v12
	s_nop 1
	v_mov_b32_dpp v14, v12 row_half_mirror row_mask:0xf bank_mask:0xf
	s_waitcnt lgkmcnt(0)
	v_max_f32_e32 v14, v14, v14
	v_max_f32_e32 v12, v12, v14
	s_nop 1
	v_mov_b32_dpp v14, v12 row_mirror row_mask:0xf bank_mask:0xf
	s_waitcnt lgkmcnt(0)
	v_max_f32_e32 v14, v14, v14
	v_max_f32_e32 v12, v12, v14
	v_sub_f32_e32 v14, v31, v12
	v_sub_f32_e32 v27, v32, v12
	v_sub_f32_e32 v28, v33, v12
	v_sub_f32_e32 v12, v34, v12
	global_load_dword v33, v[4:5], off offset:768
	global_load_dword v34, v[4:5], off offset:832
	global_load_dword v39, v[4:5], off offset:896
	global_load_dword v40, v[4:5], off offset:960
	v_exp_f32_e32 v14, v14
	v_exp_f32_e32 v27, v27
	v_exp_f32_e32 v28, v28
	v_exp_f32_e32 v12, v12
	v_add_f32_e32 v29, 0, v14
	v_add_f32_e32 v29, v29, v27
	v_add_f32_e32 v29, v29, v28
	v_add_f32_e32 v29, v29, v12
	s_nop 1
	v_mov_b32_dpp v30, v29 quad_perm:[1,0,3,2] row_mask:0xf bank_mask:0xf
	v_accvgpr_read_b32 v31, a13
	s_waitcnt vmcnt(8)
	v_fmac_f32_e32 v38, 0x3e0293ee, v31
	v_max_f32_e32 v26, v37, v38
	v_max3_f32 v26, v35, v36, v26
	s_waitcnt lgkmcnt(0)
	v_add_f32_e32 v22, v29, v30
	s_nop 1
	v_mov_b32_dpp v29, v26 quad_perm:[1,0,3,2] row_mask:0xf bank_mask:0xf
	v_accvgpr_read_b32 v32, a10
	s_nop 1
	v_mov_b32_dpp v25, v22 quad_perm:[2,3,0,1] row_mask:0xf bank_mask:0xf
	v_accvgpr_read_b32 v30, a6
	v_accvgpr_read_b32 v4, a11
	s_waitcnt lgkmcnt(1)
	v_max_f32_e32 v29, v29, v29
	v_max_f32_e32 v26, v26, v29
	s_nop 1
	v_mov_b32_dpp v29, v26 quad_perm:[2,3,0,1] row_mask:0xf bank_mask:0xf
	s_waitcnt lgkmcnt(1)
	v_add_f32_e32 v22, v22, v25
	s_nop 1
	v_mov_b32_dpp v25, v22 row_half_mirror row_mask:0xf bank_mask:0xf
	v_accvgpr_read_b32 v31, a7
	v_cvt_f16_f32_e32 v14, v14
	s_waitcnt lgkmcnt(1)
	v_max_f32_e32 v5, v29, v29
	v_max_f32_e32 v5, v26, v5
	s_nop 1
	v_mov_b32_dpp v26, v5 row_half_mirror row_mask:0xf bank_mask:0xf
	s_waitcnt lgkmcnt(1)
	v_add_f32_e32 v22, v22, v25
	s_nop 1
	v_mov_b32_dpp v25, v22 row_mirror row_mask:0xf bank_mask:0xf
	v_cvt_f16_f32_e32 v27, v27
	v_cvt_f16_f32_e32 v28, v28
	s_waitcnt lgkmcnt(1)
	v_max_f32_e32 v26, v26, v26
	v_max_f32_e32 v5, v5, v26
	s_nop 1
	v_mov_b32_dpp v26, v5 row_mirror row_mask:0xf bank_mask:0xf
	s_waitcnt lgkmcnt(1)
	v_add_f32_e32 v22, v22, v25
	v_div_scale_f32 v25, s[6:7], v22, v22, 1.0
	v_rcp_f32_e32 v29, v25
	s_waitcnt lgkmcnt(0)
	v_max_f32_e32 v26, v26, v26
	v_max_f32_e32 v5, v5, v26
	v_sub_f32_e32 v26, v35, v5
	v_fma_f32 v43, -v25, v29, 1.0
	v_exp_f32_e32 v26, v26
	v_sub_f32_e32 v35, v36, v5
	v_fmac_f32_e32 v29, v43, v29
	v_exp_f32_e32 v35, v35
	v_sub_f32_e32 v36, v37, v5
	v_exp_f32_e32 v36, v36
	v_sub_f32_e32 v5, v38, v5
	v_exp_f32_e32 v5, v5
	v_add_f32_e32 v37, 0, v26
	v_add_f32_e32 v37, v37, v35
	v_add_f32_e32 v37, v37, v36
	v_add_f32_e32 v37, v37, v5
	s_waitcnt vmcnt(7)
	v_fmac_f32_e32 v15, 0x3e0293ee, v23
	s_waitcnt vmcnt(6)
	v_fmac_f32_e32 v17, 0x3e0293ee, v30
	s_waitcnt vmcnt(5)
	v_fmac_f32_e32 v19, 0x3e0293ee, v32
	s_waitcnt vmcnt(4)
	v_fmac_f32_e32 v21, 0x3e0293ee, v41
	v_max_f32_e32 v23, v19, v21
	v_max3_f32 v23, v15, v17, v23
	s_nop 1
	v_mov_b32_dpp v30, v23 quad_perm:[1,0,3,2] row_mask:0xf bank_mask:0xf
	v_div_scale_f32 v32, vcc, 1.0, v22, 1.0
	v_mul_f32_e32 v41, v32, v29
	v_fma_f32 v43, -v25, v41, v32
	s_waitcnt lgkmcnt(0)
	v_max_f32_e32 v30, v30, v30
	v_max_f32_e32 v23, v23, v30
	s_nop 1
	v_mov_b32_dpp v30, v23 quad_perm:[2,3,0,1] row_mask:0xf bank_mask:0xf
	v_fmac_f32_e32 v41, v43, v29
	v_fma_f32 v25, -v25, v41, v32
	v_div_fmas_f32 v25, v25, v29, v41
	s_nop 1
	v_mov_b32_dpp v38, v37 quad_perm:[1,0,3,2] row_mask:0xf bank_mask:0xf
	s_waitcnt lgkmcnt(1)
	v_max_f32_e32 v30, v30, v30
	v_max_f32_e32 v23, v23, v30
	s_nop 1
	v_mov_b32_dpp v30, v23 row_half_mirror row_mask:0xf bank_mask:0xf
	s_waitcnt vmcnt(3)
	v_fmac_f32_e32 v33, 0x3e0293ee, v24
	s_waitcnt vmcnt(1)
	v_fmac_f32_e32 v39, 0x3e0293ee, v4
	s_waitcnt vmcnt(0)
	v_fmac_f32_e32 v40, 0x3e0293ee, v42
	v_fmac_f32_e32 v34, 0x3e0293ee, v31
	s_waitcnt lgkmcnt(0)
	v_max_f32_e32 v30, v30, v30
	v_max_f32_e32 v23, v23, v30
	s_nop 1
	v_mov_b32_dpp v30, v23 row_mirror row_mask:0xf bank_mask:0xf
	v_max_f32_e32 v4, v39, v40
	v_max3_f32 v4, v33, v34, v4
	v_add_f32_e32 v37, v37, v38
	s_nop 1
	v_mov_b32_dpp v38, v37 quad_perm:[2,3,0,1] row_mask:0xf bank_mask:0xf
	s_waitcnt lgkmcnt(1)
	v_max_f32_e32 v29, v30, v30
	v_max_f32_e32 v23, v23, v29
	v_sub_f32_e32 v15, v15, v23
	v_sub_f32_e32 v17, v17, v23
	v_sub_f32_e32 v19, v19, v23
	v_sub_f32_e32 v21, v21, v23
	s_nop 1
	v_mov_b32_dpp v23, v4 quad_perm:[1,0,3,2] row_mask:0xf bank_mask:0xf
	s_waitcnt lgkmcnt(1)
	v_add_f32_e32 v37, v37, v38
	s_nop 1
	v_mov_b32_dpp v38, v37 row_half_mirror row_mask:0xf bank_mask:0xf
	v_exp_f32_e32 v15, v15
	v_exp_f32_e32 v17, v17
	s_waitcnt lgkmcnt(1)
	v_max_f32_e32 v23, v23, v23
	v_max_f32_e32 v4, v4, v23
	s_nop 1
	v_mov_b32_dpp v23, v4 quad_perm:[2,3,0,1] row_mask:0xf bank_mask:0xf
	s_waitcnt lgkmcnt(1)
	v_add_f32_e32 v32, v37, v38
	s_nop 1
	v_mov_b32_dpp v37, v32 row_mirror row_mask:0xf bank_mask:0xf
	v_div_fixup_f32 v22, v25, v22, 1.0
	v_exp_f32_e32 v19, v19
	s_waitcnt lgkmcnt(1)
	v_max_f32_e32 v23, v23, v23
	v_max_f32_e32 v4, v4, v23
	s_nop 1
	v_mov_b32_dpp v23, v4 row_half_mirror row_mask:0xf bank_mask:0xf
	s_waitcnt lgkmcnt(1)
	v_add_f32_e32 v25, v32, v37
	v_div_scale_f32 v29, s[6:7], v25, v25, 1.0
	v_exp_f32_e32 v21, v21
	s_waitcnt lgkmcnt(0)
	v_max_f32_e32 v23, v23, v23
	v_max_f32_e32 v4, v4, v23
	s_nop 1
	v_mov_b32_dpp v23, v4 row_mirror row_mask:0xf bank_mask:0xf
	v_rcp_f32_e32 v30, v29
	v_add_f32_e32 v32, 0, v15
	v_add_f32_e32 v24, v32, v17
	v_add_f32_e32 v24, v24, v19
	s_waitcnt lgkmcnt(0)
	v_max_f32_e32 v23, v23, v23
	v_max_f32_e32 v4, v4, v23
	v_add_f32_e32 v24, v24, v21
	v_sub_f32_e32 v23, v33, v4
	s_nop 1
	v_mov_b32_dpp v31, v24 quad_perm:[1,0,3,2] row_mask:0xf bank_mask:0xf
	v_fma_f32 v32, -v29, v30, 1.0
	v_exp_f32_e32 v23, v23
	v_sub_f32_e32 v33, v34, v4
	v_fmac_f32_e32 v30, v32, v30
	v_div_scale_f32 v32, vcc, 1.0, v25, 1.0
	v_exp_f32_e32 v33, v33
	v_sub_f32_e32 v34, v39, v4
	v_mul_f32_e32 v37, v32, v30
	v_exp_f32_e32 v34, v34
	v_sub_f32_e32 v4, v40, v4
	v_fma_f32 v38, -v29, v37, v32
	v_exp_f32_e32 v4, v4
	v_fmac_f32_e32 v37, v38, v30
	v_add_f32_e32 v38, 0, v23
	s_waitcnt lgkmcnt(0)
	v_add_f32_e32 v24, v24, v31
	v_add_f32_e32 v38, v38, v33
	s_nop 1
	v_mov_b32_dpp v31, v24 quad_perm:[2,3,0,1] row_mask:0xf bank_mask:0xf
	v_add_f32_e32 v38, v38, v34
	v_add_f32_e32 v38, v38, v4
	s_nop 1
	v_mov_b32_dpp v13, v38 quad_perm:[1,0,3,2] row_mask:0xf bank_mask:0xf
	v_fma_f32 v29, -v29, v37, v32
	s_waitcnt lgkmcnt(1)
	v_add_f32_e32 v24, v24, v31
	s_nop 1
	v_mov_b32_dpp v31, v24 row_half_mirror row_mask:0xf bank_mask:0xf
	v_div_fmas_f32 v29, v29, v30, v37
	s_waitcnt lgkmcnt(1)
	v_add_f32_e32 v13, v38, v13
	s_nop 1
	v_mov_b32_dpp v16, v13 quad_perm:[2,3,0,1] row_mask:0xf bank_mask:0xf
	v_div_fixup_f32 v25, v29, v25, 1.0
	s_waitcnt lgkmcnt(1)
	v_add_f32_e32 v24, v24, v31
	s_nop 1
	v_mov_b32_dpp v31, v24 row_mirror row_mask:0xf bank_mask:0xf
	v_cvt_f16_f32_e32 v12, v12
	s_waitcnt lgkmcnt(1)
	v_add_f32_e32 v13, v13, v16
	s_nop 1
	v_mov_b32_dpp v10, v13 row_half_mirror row_mask:0xf bank_mask:0xf
	v_cvt_f16_f32_e32 v26, v26
	s_waitcnt lgkmcnt(1)
	v_add_f32_e32 v24, v24, v31
	v_div_scale_f32 v30, s[6:7], v24, v24, 1.0
	v_rcp_f32_e32 v31, v30
	s_waitcnt lgkmcnt(0)
	v_add_f32_e32 v10, v13, v10
	s_nop 1
	v_mov_b32_dpp v11, v10 row_mirror row_mask:0xf bank_mask:0xf
	v_cvt_f16_f32_e32 v5, v5
	v_fma_f32 v16, -v30, v31, 1.0
	v_fmac_f32_e32 v31, v16, v31
	v_div_scale_f32 v16, vcc, 1.0, v24, 1.0
	v_mul_f32_e32 v13, v16, v31
	s_waitcnt lgkmcnt(0)
	v_add_f32_e32 v10, v10, v11
	v_fma_f32 v29, -v30, v13, v16
	v_div_scale_f32 v11, s[6:7], v10, v10, 1.0
	v_fmac_f32_e32 v13, v29, v31
	v_rcp_f32_e32 v29, v11
	v_fma_f32 v16, -v30, v13, v16
	v_div_fmas_f32 v13, v16, v31, v13
	v_div_fixup_f32 v13, v13, v24, 1.0
	v_fma_f32 v16, -v11, v29, 1.0
	v_fmac_f32_e32 v29, v16, v29
	v_mov_b32_e32 v16, 0x8c00
	v_mad_u32_u24 v16, v1, s4, v16
	v_lshlrev_b32_e32 v24, 1, v8
	v_or_b32_e32 v30, v16, v24
	s_movk_i32 s4, 0x240
	v_mad_u32_u24 v31, v7, s4, v30
	ds_write_b16 v31, v14
	ds_write_b16 v31, v27 offset:32
	ds_write_b16 v31, v28 offset:64
	ds_write_b16 v31, v12 offset:96
	v_cvt_f16_f32_e32 v27, v35
	v_or_b32_e32 v12, 1, v9
	s_movk_i32 s4, 0x90
	v_cvt_f16_f32_e32 v28, v36
	v_mad_u32_u24 v14, v12, s4, v30
	ds_write_b16 v14, v26
	ds_write_b16 v14, v27 offset:32
	ds_write_b16 v14, v28 offset:64
	ds_write_b16 v14, v5 offset:96
	v_cvt_f16_f32_e32 v5, v15
	v_cvt_f16_f32_e32 v15, v17
	v_cvt_f16_f32_e32 v17, v19
	v_cvt_f16_f32_e32 v19, v21
	ds_write_b16 v14, v5 offset:144
	ds_write_b16 v14, v15 offset:176
	ds_write_b16 v14, v17 offset:208
	ds_write_b16 v14, v19 offset:240
	v_cvt_f16_f32_e32 v5, v23
	v_cvt_f16_f32_e32 v15, v33
	v_cvt_f16_f32_e32 v17, v34
	v_cvt_f16_f32_e32 v4, v4
	ds_write_b16 v14, v5 offset:288
	ds_write_b16 v14, v15 offset:320
	ds_write_b16 v14, v17 offset:352
	ds_write_b16 v14, v4 offset:384
	v_mul_u32_u24_e32 v4, 0x90, v8
	v_add3_u32 v4, v16, v4, v20
	s_waitcnt lgkmcnt(0)
	s_barrier
	ds_read2_b64 v[36:39], v4 offset1:4
	ds_read2_b64 v[40:43], v4 offset0:8 offset1:12
	ds_read_b64_tr_b16 v[16:17], v0 offset:4608
	ds_read_b64_tr_b16 v[14:15], v0
	ds_read_b64_tr_b16 v[18:19], v0 offset:32
	ds_read_b64_tr_b16 v[30:31], v0 offset:64
	ds_read_b64_tr_b16 v[44:45], v0 offset:96
	ds_read_b64_tr_b16 v[20:21], v0 offset:4640
	ds_read_b64_tr_b16 v[32:33], v0 offset:4672
	ds_read_b64_tr_b16 v[46:47], v0 offset:4704
	s_waitcnt lgkmcnt(6)
	v_mfma_f32_16x16x32_f16 a[0:3], v[36:39], v[14:17], 0
	v_div_scale_f32 v4, vcc, 1.0, v10, 1.0
	v_mul_f32_e32 v5, v4, v29
	ds_read_b64_tr_b16 v[16:17], v0 offset:13824
	ds_read_b64_tr_b16 v[14:15], v0 offset:9216
	ds_read_b64_tr_b16 v[48:49], v0 offset:9248
	ds_read_b64_tr_b16 v[52:53], v0 offset:9280
	ds_read_b64_tr_b16 v[56:57], v0 offset:9312
	ds_read_b64_tr_b16 v[50:51], v0 offset:13856
	ds_read_b64_tr_b16 v[54:55], v0 offset:13888
	ds_read_b64_tr_b16 v[58:59], v0 offset:13920
	s_waitcnt lgkmcnt(6)
	v_mfma_f32_16x16x32_f16 a[0:3], v[40:43], v[14:17], a[0:3]
	v_fma_f32 v8, -v11, v5, v4
	v_fmac_f32_e32 v5, v8, v29
	v_fma_f32 v4, -v11, v5, v4
	v_mfma_f32_16x16x32_f16 a[4:7], v[36:39], v[18:21], 0
	v_div_fmas_f32 v4, v4, v29, v5
	v_div_fixup_f32 v4, v4, v10, 1.0
	s_movk_i32 s4, 0x1100
	v_mfma_f32_16x16x32_f16 a[8:11], v[36:39], v[30:33], 0
	v_accvgpr_read_b32 v5, a0
	v_accvgpr_read_b32 v8, a1
	v_accvgpr_read_b32 v9, a2
	s_waitcnt lgkmcnt(2)
	v_mfma_f32_16x16x32_f16 a[4:7], v[40:43], v[48:51], a[4:7]
	v_accvgpr_read_b32 v10, a3
	v_fma_mixlo_f16 v5, v5, v22, 0
	s_waitcnt lgkmcnt(1)
	v_mfma_f32_16x16x32_f16 a[0:3], v[40:43], v[52:55], a[8:11]
	v_mfma_f32_16x16x32_f16 a[8:11], v[36:39], v[44:47], 0
	ds_read_b64_tr_b16 v[28:29], v0 offset:4736
	ds_read_b64_tr_b16 v[26:27], v0 offset:128
	ds_read_b64_tr_b16 v[30:31], v0 offset:160
	ds_read_b64_tr_b16 v[44:45], v0 offset:192
	ds_read_b64_tr_b16 v[48:49], v0 offset:224
	ds_read_b64_tr_b16 v[32:33], v0 offset:4768
	ds_read_b64_tr_b16 v[46:47], v0 offset:4800
	ds_read_b64_tr_b16 v[50:51], v0 offset:4832
	v_accvgpr_read_b32 v11, a4
	v_accvgpr_read_b32 v14, a5
	v_accvgpr_read_b32 v15, a6
	v_accvgpr_read_b32 v16, a7
	v_accvgpr_read_b32 v17, a0
	v_accvgpr_read_b32 v18, a1
	s_waitcnt lgkmcnt(8)
	v_mfma_f32_16x16x32_f16 a[4:7], v[40:43], v[56:59], a[8:11]
	v_accvgpr_read_b32 v19, a3
	s_waitcnt lgkmcnt(6)
	v_mfma_f32_16x16x32_f16 a[8:11], v[36:39], v[26:29], 0
	ds_read_b64_tr_b16 v[28:29], v0 offset:13952
	ds_read_b64_tr_b16 v[26:27], v0 offset:9344
	ds_read_b64_tr_b16 v[52:53], v0 offset:9376
	ds_read_b64_tr_b16 v[56:57], v0 offset:9408
	ds_read_b64_tr_b16 v[60:61], v0 offset:9440
	ds_read_b64_tr_b16 v[54:55], v0 offset:13984
	ds_read_b64_tr_b16 v[58:59], v0 offset:14016
	ds_read_b64_tr_b16 v[62:63], v0 offset:14048
	v_accvgpr_read_b32 v0, a2
	v_accvgpr_read_b32 v20, a4
	s_waitcnt lgkmcnt(10)
	v_mfma_f32_16x16x32_f16 a[0:3], v[36:39], v[30:33], 0
	v_accvgpr_read_b32 v21, a5
	v_accvgpr_read_b32 v23, a6
	v_fma_mixlo_f16 v0, v0, v13, 0
	s_waitcnt lgkmcnt(2)
	v_mfma_f32_16x16x32_f16 a[0:3], v[40:43], v[52:55], a[0:3]
	v_mfma_f32_16x16x32_f16 a[8:11], v[40:43], v[26:29], a[8:11]
	v_accvgpr_read_b32 v26, a7
	v_mfma_f32_16x16x32_f16 a[4:7], v[36:39], v[44:47], 0
	s_nop 4
	v_accvgpr_read_b32 v31, a0
	v_accvgpr_read_b32 v32, a1
	v_accvgpr_read_b32 v33, a2
	v_accvgpr_read_b32 v34, a3
	v_mfma_f32_16x16x32_f16 a[0:3], v[36:39], v[48:51], 0
	v_accvgpr_read_b32 v27, a8
	v_accvgpr_read_b32 v28, a9
	v_accvgpr_read_b32 v29, a10
	s_waitcnt lgkmcnt(1)
	v_mfma_f32_16x16x32_f16 a[4:7], v[40:43], v[56:59], a[4:7]
	v_accvgpr_read_b32 v30, a11
	s_waitcnt lgkmcnt(0)
	v_mfma_f32_16x16x32_f16 a[0:3], v[40:43], v[60:63], a[0:3]
	v_mov_b32_e32 v43, 0x4800
	v_mad_u32_u24 v43, v1, s4, v43
	v_or_b32_e32 v1, v43, v24
	s_movk_i32 s4, 0x440
	v_mad_u32_u24 v24, v7, s4, v1
	ds_write_b16 v24, v5
	v_fma_mixlo_f16 v5, v8, v25, 0
	v_mad_u32_u24 v1, v12, s3, v1
	ds_write_b16 v1, v5
	v_fma_mixlo_f16 v5, v9, v13, 0
	ds_write_b16 v1, v5 offset:272
	v_fma_mixlo_f16 v5, v10, v4, 0
	ds_write_b16 v1, v5 offset:544
	v_fma_mixlo_f16 v5, v11, v22, 0
	ds_write_b16 v24, v5 offset:32
	v_fma_mixlo_f16 v5, v14, v25, 0
	ds_write_b16 v1, v5 offset:32
	v_fma_mixlo_f16 v5, v15, v13, 0
	ds_write_b16 v1, v5 offset:304
	v_fma_mixlo_f16 v5, v16, v4, 0
	ds_write_b16 v1, v5 offset:576
	v_fma_mixlo_f16 v5, v17, v22, 0
	ds_write_b16 v24, v5 offset:64
	ds_write_b16 v1, v0 offset:336
	v_fma_mixlo_f16 v0, v19, v4, 0
	v_fma_mixlo_f16 v5, v18, v25, 0
	ds_write_b16 v1, v0 offset:608
	v_fma_mixlo_f16 v0, v20, v22, 0
	ds_write_b16 v1, v5 offset:64
	ds_write_b16 v24, v0 offset:96
	v_fma_mixlo_f16 v0, v21, v25, 0
	ds_write_b16 v1, v0 offset:96
	v_fma_mixlo_f16 v0, v23, v13, 0
	ds_write_b16 v1, v0 offset:368
	v_fma_mixlo_f16 v0, v26, v4, 0
	ds_write_b16 v1, v0 offset:640
	v_fma_mixlo_f16 v0, v27, v22, 0
	ds_write_b16 v24, v0 offset:128
	v_fma_mixlo_f16 v0, v28, v25, 0
	ds_write_b16 v1, v0 offset:128
	v_fma_mixlo_f16 v0, v29, v13, 0
	ds_write_b16 v1, v0 offset:400
	v_fma_mixlo_f16 v0, v30, v4, 0
	ds_write_b16 v1, v0 offset:672
	v_fma_mixlo_f16 v0, v31, v22, 0
	ds_write_b16 v24, v0 offset:160
	v_fma_mixlo_f16 v0, v32, v25, 0
	ds_write_b16 v1, v0 offset:160
	v_fma_mixlo_f16 v0, v33, v13, 0
	v_accvgpr_read_b32 v35, a4
	ds_write_b16 v1, v0 offset:432
	v_fma_mixlo_f16 v0, v34, v4, 0
	v_accvgpr_read_b32 v36, a5
	ds_write_b16 v1, v0 offset:704
	v_fma_mixlo_f16 v0, v35, v22, 0
	v_accvgpr_read_b32 v37, a6
	ds_write_b16 v24, v0 offset:192
	v_fma_mixlo_f16 v0, v36, v25, 0
	v_accvgpr_read_b32 v38, a7
	ds_write_b16 v1, v0 offset:192
	v_fma_mixlo_f16 v0, v37, v13, 0
	v_accvgpr_read_b32 v39, a0
	ds_write_b16 v1, v0 offset:464
	v_fma_mixlo_f16 v0, v38, v4, 0
	v_accvgpr_read_b32 v40, a1
	ds_write_b16 v1, v0 offset:736
	v_fma_mixlo_f16 v0, v39, v22, 0
	v_accvgpr_read_b32 v41, a2
	ds_write_b16 v24, v0 offset:224
	v_fma_mixlo_f16 v0, v40, v25, 0
	v_accvgpr_read_b32 v42, a3
	ds_write_b16 v1, v0 offset:224
	v_fma_mixlo_f16 v0, v41, v13, 0
	ds_write_b16 v1, v0 offset:496
	v_fma_mixlo_f16 v0, v42, v4, 0
	ds_write_b16 v1, v0 offset:768
	v_lshl_or_b32 v4, s2, 6, v6
	s_movk_i32 s2, 0x600
	v_mov_b64_e32 v[0:1], s[8:9]
	v_mad_i64_i32 v[0:1], s[4:5], v4, s2, v[0:1]
	v_lshl_add_u64 v[0:1], v[0:1], 0, s[0:1]
	v_or_b32_e32 v4, v43, v2
	v_lshl_add_u64 v[0:1], v[0:1], 0, v[2:3]
	v_mul_u32_u24_e32 v2, 0x300, v7
	v_mad_u32_u24 v6, v7, s3, v4
	v_lshlrev_b32_e32 v2, 1, v2
	s_waitcnt lgkmcnt(0)
	ds_read_b128 v[8:11], v6
	v_lshl_add_u64 v[12:13], v[0:1], 0, v[2:3]
	ds_read_b128 v[0:3], v6 offset:1088
	s_movk_i32 s0, 0x1000
	v_add_co_u32_e32 v4, vcc, s0, v12
	s_waitcnt lgkmcnt(1)
	global_store_dwordx4 v[12:13], v[8:11], off nt
	v_addc_co_u32_e32 v5, vcc, 0, v13, vcc
	s_waitcnt lgkmcnt(0)
	global_store_dwordx4 v[4:5], v[0:3], off offset:2048 nt
	ds_read_b128 v[0:3], v6 offset:2176
	ds_read_b128 v[4:7], v6 offset:3264
	v_add_co_u32_e32 v8, vcc, 0x3000, v12
	s_nop 1
	v_addc_co_u32_e32 v9, vcc, 0, v13, vcc
	s_waitcnt lgkmcnt(1)
	global_store_dwordx4 v[8:9], v[0:3], off nt
	s_nop 1
	v_add_co_u32_e32 v0, vcc, 0x4000, v12
	s_nop 1
	v_addc_co_u32_e32 v1, vcc, 0, v13, vcc
	s_waitcnt lgkmcnt(0)
	global_store_dwordx4 v[0:1], v[4:7], off offset:2048 nt
	s_endpgm
